# speedup vs baseline: 1.0913x; 1.0913x over previous
_Z8dog_mainPKfS0_S0_S0_S0_S0_S0_Pf:
	s_load_dwordx8 s[12:19], s[0:1], 0x0
	s_load_dwordx8 s[20:27], s[0:1], 0x20
	s_and_b32 s3, s2, 7
	s_lshl_b32 s3, s3, 5
	s_lshr_b32 s4, s2, 3
	s_add_i32 s4, s3, s4
	s_and_b32 s6, s4, 3
	s_lshr_b32 s7, s4, 2
	s_mov_b32 s5, 0
	s_lshl_b64 s[8:9], s[4:5], 18
	v_and_b32_e32 v1, 63, v0
	v_lshrrev_b32_e32 v2, 6, v0
	v_and_b32_e32 v3, 31, v0
	v_lshl_or_b32 v4, v2, 5, v3
	v_lshlrev_b32_e32 v5, 2, v4
	v_lshlrev_b32_e32 v6, 4, v1
	v_lshl_or_b32 v6, v2, 12, v6
	v_readfirstlane_b32 s28, v2
	s_waitcnt lgkmcnt(0)
	global_load_dword v20, v5, s[18:19]
	global_load_dword v21, v5, s[20:21]
	global_load_dword v22, v5, s[22:23]
	global_load_dword v23, v5, s[24:25]
	global_load_dword v24, v5, s[14:15]
	global_load_dword v25, v5, s[16:17]
	s_add_u32 s12, s12, s8
	s_addc_u32 s13, s13, s9
.Lloads:
	global_load_dwordx4 v[128:131], v6, s[12:13] offset:0 nt
	global_load_dwordx4 v[132:135], v6, s[12:13] offset:1024 nt
	global_load_dwordx4 v[136:139], v6, s[12:13] offset:2048 nt
	global_load_dwordx4 v[140:143], v6, s[12:13] offset:3072 nt
	v_add_u32_e32 v6, 0x8000, v6
	global_load_dwordx4 v[144:147], v6, s[12:13] offset:0 nt
	global_load_dwordx4 v[148:151], v6, s[12:13] offset:1024 nt
	global_load_dwordx4 v[152:155], v6, s[12:13] offset:2048 nt
	global_load_dwordx4 v[156:159], v6, s[12:13] offset:3072 nt
	v_add_u32_e32 v6, 0x8000, v6
	global_load_dwordx4 v[160:163], v6, s[12:13] offset:0 nt
	global_load_dwordx4 v[164:167], v6, s[12:13] offset:1024 nt
	global_load_dwordx4 v[168:171], v6, s[12:13] offset:2048 nt
	global_load_dwordx4 v[172:175], v6, s[12:13] offset:3072 nt
	v_add_u32_e32 v6, 0x8000, v6
	global_load_dwordx4 v[176:179], v6, s[12:13] offset:0 nt
	global_load_dwordx4 v[180:183], v6, s[12:13] offset:1024 nt
	global_load_dwordx4 v[184:187], v6, s[12:13] offset:2048 nt
	global_load_dwordx4 v[188:191], v6, s[12:13] offset:3072 nt
.Lsetup:
	v_bfe_u32 v7, v0, 5, 1
	v_and_b32_e32 v16, 1, v0
	v_cmp_eq_u32_e64 s[30:31], 0, v16
	v_and_b32_e32 v17, 2, v0
	v_cmp_eq_u32_e64 s[32:33], 0, v17
	v_and_b32_e32 v16, 3, v0
	v_lshrrev_b32_e32 v17, 2, v1
	v_lshlrev_b32_e32 v16, 5, v16
	v_lshl_add_u32 v16, v17, 1, v16
	v_lshrrev_b32_e32 v17, 1, v2
	s_movk_i32 s10, 0x110
	v_mad_u32_u24 v16, v17, s10, v16
	v_and_b32_e32 v17, 1, v2
	v_lshl_add_u32 v14, v17, 7, v16
	v_lshlrev_b32_e32 v17, 4, v7
	v_mad_u32_u24 v15, v3, s10, v17
	s_lshl_b32 s11, s6, 5
	v_lshl_add_u32 v18, v7, 2, s11
	v_cvt_f32_u32_e32 v18, v18
	v_lshlrev_b32_e32 v19, 3, v7
	v_cvt_f32_u32_e32 v19, v19
	s_waitcnt vmcnt(16)
	v_add_f32_e32 v26, v20, v21
	v_rcp_f32_e32 v27, v20
	v_rcp_f32_e32 v28, v26
	v_sub_f32_e32 v12, v19, v22
	v_sub_f32_e32 v13, v18, v23
	v_fma_f32 v29, -v20, v27, 1.0
	v_fma_f32 v30, -v26, v28, 1.0
	v_fma_f32 v27, v29, v27, v27
	v_fma_f32 v28, v30, v28, v28
	v_mul_f32_e32 v8, 0xbf38aa3b, v27
	v_mul_f32_e32 v9, 0xbf38aa3b, v28
	v_mul_f32_e32 v29, v24, v27
	v_mul_f32_e32 v30, v25, v28
	v_mul_f32_e32 v10, 0x3e22f983, v29
	v_mul_f32_e32 v11, 0x3e22f983, v30
	v_mul_f32_e32 v16, v12, v12
	v_add_f32_e32 v17, 0x3f800000, v12
	v_add_f32_e32 v18, 0x40000000, v12
	v_add_f32_e32 v19, 0x40400000, v12
	v_mul_f32_e32 v17, v17, v17
	v_mul_f32_e32 v18, v18, v18
	v_mul_f32_e32 v19, v19, v19
	v_mul_f32_e32 v20, v8, v16
	v_mul_f32_e32 v24, v9, v16
	v_mul_f32_e32 v21, v8, v17
	v_mul_f32_e32 v25, v9, v17
	v_mul_f32_e32 v22, v8, v18
	v_mul_f32_e32 v26, v9, v18
	v_mul_f32_e32 v23, v8, v19
	v_mul_f32_e32 v27, v9, v19
	v_exp_f32_e32 v20, v20
	v_exp_f32_e32 v21, v21
	v_exp_f32_e32 v22, v22
	v_exp_f32_e32 v23, v23
	v_exp_f32_e32 v24, v24
	v_exp_f32_e32 v25, v25
	v_exp_f32_e32 v26, v26
	v_exp_f32_e32 v27, v27
	v_cvt_pk_f16_f32 v32, v20, v21
	v_cvt_pk_f16_f32 v33, v22, v23
	v_cvt_pk_f16_f32 v64, v24, v25
	v_cvt_pk_f16_f32 v65, v26, v27
	v_add_f32_e32 v16, 0x40800000, v12
	v_add_f32_e32 v17, 0x40a00000, v12
	v_add_f32_e32 v18, 0x40c00000, v12
	v_add_f32_e32 v19, 0x40e00000, v12
	v_mul_f32_e32 v16, v16, v16
	v_mul_f32_e32 v17, v17, v17
	v_mul_f32_e32 v18, v18, v18
	v_mul_f32_e32 v19, v19, v19
	v_mul_f32_e32 v20, v8, v16
	v_mul_f32_e32 v24, v9, v16
	v_mul_f32_e32 v21, v8, v17
	v_mul_f32_e32 v25, v9, v17
	v_mul_f32_e32 v22, v8, v18
	v_mul_f32_e32 v26, v9, v18
	v_mul_f32_e32 v23, v8, v19
	v_mul_f32_e32 v27, v9, v19
	v_exp_f32_e32 v20, v20
	v_exp_f32_e32 v21, v21
	v_exp_f32_e32 v22, v22
	v_exp_f32_e32 v23, v23
	v_exp_f32_e32 v24, v24
	v_exp_f32_e32 v25, v25
	v_exp_f32_e32 v26, v26
	v_exp_f32_e32 v27, v27
	v_cvt_pk_f16_f32 v34, v20, v21
	v_cvt_pk_f16_f32 v35, v22, v23
	v_cvt_pk_f16_f32 v66, v24, v25
	v_cvt_pk_f16_f32 v67, v26, v27
	v_add_u32_e32 v6, 0x8000, v6
	global_load_dwordx4 v[192:195], v6, s[12:13] offset:0 nt
	global_load_dwordx4 v[196:199], v6, s[12:13] offset:1024 nt
	global_load_dwordx4 v[200:203], v6, s[12:13] offset:2048 nt
	global_load_dwordx4 v[204:207], v6, s[12:13] offset:3072 nt
	v_add_f32_e32 v16, 0x41800000, v12
	v_add_f32_e32 v17, 0x41880000, v12
	v_add_f32_e32 v18, 0x41900000, v12
	v_add_f32_e32 v19, 0x41980000, v12
	v_mul_f32_e32 v16, v16, v16
	v_mul_f32_e32 v17, v17, v17
	v_mul_f32_e32 v18, v18, v18
	v_mul_f32_e32 v19, v19, v19
	v_mul_f32_e32 v20, v8, v16
	v_mul_f32_e32 v24, v9, v16
	v_mul_f32_e32 v21, v8, v17
	v_mul_f32_e32 v25, v9, v17
	v_mul_f32_e32 v22, v8, v18
	v_mul_f32_e32 v26, v9, v18
	v_mul_f32_e32 v23, v8, v19
	v_mul_f32_e32 v27, v9, v19
	v_exp_f32_e32 v20, v20
	v_exp_f32_e32 v21, v21
	v_exp_f32_e32 v22, v22
	v_exp_f32_e32 v23, v23
	v_exp_f32_e32 v24, v24
	v_exp_f32_e32 v25, v25
	v_exp_f32_e32 v26, v26
	v_exp_f32_e32 v27, v27
	v_cvt_pk_f16_f32 v36, v20, v21
	v_cvt_pk_f16_f32 v37, v22, v23
	v_cvt_pk_f16_f32 v68, v24, v25
	v_cvt_pk_f16_f32 v69, v26, v27
	v_add_f32_e32 v16, 0x41a00000, v12
	v_add_f32_e32 v17, 0x41a80000, v12
	v_add_f32_e32 v18, 0x41b00000, v12
	v_add_f32_e32 v19, 0x41b80000, v12
	v_mul_f32_e32 v16, v16, v16
	v_mul_f32_e32 v17, v17, v17
	v_mul_f32_e32 v18, v18, v18
	v_mul_f32_e32 v19, v19, v19
	v_mul_f32_e32 v20, v8, v16
	v_mul_f32_e32 v24, v9, v16
	v_mul_f32_e32 v21, v8, v17
	v_mul_f32_e32 v25, v9, v17
	v_mul_f32_e32 v22, v8, v18
	v_mul_f32_e32 v26, v9, v18
	v_mul_f32_e32 v23, v8, v19
	v_mul_f32_e32 v27, v9, v19
	v_exp_f32_e32 v20, v20
	v_exp_f32_e32 v21, v21
	v_exp_f32_e32 v22, v22
	v_exp_f32_e32 v23, v23
	v_exp_f32_e32 v24, v24
	v_exp_f32_e32 v25, v25
	v_exp_f32_e32 v26, v26
	v_exp_f32_e32 v27, v27
	v_cvt_pk_f16_f32 v38, v20, v21
	v_cvt_pk_f16_f32 v39, v22, v23
	v_cvt_pk_f16_f32 v70, v24, v25
	v_cvt_pk_f16_f32 v71, v26, v27
	v_add_u32_e32 v6, 0x8000, v6
	global_load_dwordx4 v[208:211], v6, s[12:13] offset:0 nt
	global_load_dwordx4 v[212:215], v6, s[12:13] offset:1024 nt
	global_load_dwordx4 v[216:219], v6, s[12:13] offset:2048 nt
	global_load_dwordx4 v[220:223], v6, s[12:13] offset:3072 nt
	v_add_f32_e32 v16, 0x42000000, v12
	v_add_f32_e32 v17, 0x42040000, v12
	v_add_f32_e32 v18, 0x42080000, v12
	v_add_f32_e32 v19, 0x420c0000, v12
	v_mul_f32_e32 v16, v16, v16
	v_mul_f32_e32 v17, v17, v17
	v_mul_f32_e32 v18, v18, v18
	v_mul_f32_e32 v19, v19, v19
	v_mul_f32_e32 v20, v8, v16
	v_mul_f32_e32 v24, v9, v16
	v_mul_f32_e32 v21, v8, v17
	v_mul_f32_e32 v25, v9, v17
	v_mul_f32_e32 v22, v8, v18
	v_mul_f32_e32 v26, v9, v18
	v_mul_f32_e32 v23, v8, v19
	v_mul_f32_e32 v27, v9, v19
	v_exp_f32_e32 v20, v20
	v_exp_f32_e32 v21, v21
	v_exp_f32_e32 v22, v22
	v_exp_f32_e32 v23, v23
	v_exp_f32_e32 v24, v24
	v_exp_f32_e32 v25, v25
	v_exp_f32_e32 v26, v26
	v_exp_f32_e32 v27, v27
	v_cvt_pk_f16_f32 v40, v20, v21
	v_cvt_pk_f16_f32 v41, v22, v23
	v_cvt_pk_f16_f32 v72, v24, v25
	v_cvt_pk_f16_f32 v73, v26, v27
	v_add_f32_e32 v16, 0x42100000, v12
	v_add_f32_e32 v17, 0x42140000, v12
	v_add_f32_e32 v18, 0x42180000, v12
	v_add_f32_e32 v19, 0x421c0000, v12
	v_mul_f32_e32 v16, v16, v16
	v_mul_f32_e32 v17, v17, v17
	v_mul_f32_e32 v18, v18, v18
	v_mul_f32_e32 v19, v19, v19
	v_mul_f32_e32 v20, v8, v16
	v_mul_f32_e32 v24, v9, v16
	v_mul_f32_e32 v21, v8, v17
	v_mul_f32_e32 v25, v9, v17
	v_mul_f32_e32 v22, v8, v18
	v_mul_f32_e32 v26, v9, v18
	v_mul_f32_e32 v23, v8, v19
	v_mul_f32_e32 v27, v9, v19
	v_exp_f32_e32 v20, v20
	v_exp_f32_e32 v21, v21
	v_exp_f32_e32 v22, v22
	v_exp_f32_e32 v23, v23
	v_exp_f32_e32 v24, v24
	v_exp_f32_e32 v25, v25
	v_exp_f32_e32 v26, v26
	v_exp_f32_e32 v27, v27
	v_cvt_pk_f16_f32 v42, v20, v21
	v_cvt_pk_f16_f32 v43, v22, v23
	v_cvt_pk_f16_f32 v74, v24, v25
	v_cvt_pk_f16_f32 v75, v26, v27
	v_add_u32_e32 v6, 0x8000, v6
	global_load_dwordx4 v[224:227], v6, s[12:13] offset:0 nt
	global_load_dwordx4 v[228:231], v6, s[12:13] offset:1024 nt
	global_load_dwordx4 v[232:235], v6, s[12:13] offset:2048 nt
	global_load_dwordx4 v[236:239], v6, s[12:13] offset:3072 nt
	v_add_f32_e32 v16, 0x42400000, v12
	v_add_f32_e32 v17, 0x42440000, v12
	v_add_f32_e32 v18, 0x42480000, v12
	v_add_f32_e32 v19, 0x424c0000, v12
	v_mul_f32_e32 v16, v16, v16
	v_mul_f32_e32 v17, v17, v17
	v_mul_f32_e32 v18, v18, v18
	v_mul_f32_e32 v19, v19, v19
	v_mul_f32_e32 v20, v8, v16
	v_mul_f32_e32 v24, v9, v16
	v_mul_f32_e32 v21, v8, v17
	v_mul_f32_e32 v25, v9, v17
	v_mul_f32_e32 v22, v8, v18
	v_mul_f32_e32 v26, v9, v18
	v_mul_f32_e32 v23, v8, v19
	v_mul_f32_e32 v27, v9, v19
	v_exp_f32_e32 v20, v20
	v_exp_f32_e32 v21, v21
	v_exp_f32_e32 v22, v22
	v_exp_f32_e32 v23, v23
	v_exp_f32_e32 v24, v24
	v_exp_f32_e32 v25, v25
	v_exp_f32_e32 v26, v26
	v_exp_f32_e32 v27, v27
	v_cvt_pk_f16_f32 v44, v20, v21
	v_cvt_pk_f16_f32 v45, v22, v23
	v_cvt_pk_f16_f32 v76, v24, v25
	v_cvt_pk_f16_f32 v77, v26, v27
	v_add_f32_e32 v16, 0x42500000, v12
	v_add_f32_e32 v17, 0x42540000, v12
	v_add_f32_e32 v18, 0x42580000, v12
	v_add_f32_e32 v19, 0x425c0000, v12
	v_mul_f32_e32 v16, v16, v16
	v_mul_f32_e32 v17, v17, v17
	v_mul_f32_e32 v18, v18, v18
	v_mul_f32_e32 v19, v19, v19
	v_mul_f32_e32 v20, v8, v16
	v_mul_f32_e32 v24, v9, v16
	v_mul_f32_e32 v21, v8, v17
	v_mul_f32_e32 v25, v9, v17
	v_mul_f32_e32 v22, v8, v18
	v_mul_f32_e32 v26, v9, v18
	v_mul_f32_e32 v23, v8, v19
	v_mul_f32_e32 v27, v9, v19
	v_exp_f32_e32 v20, v20
	v_exp_f32_e32 v21, v21
	v_exp_f32_e32 v22, v22
	v_exp_f32_e32 v23, v23
	v_exp_f32_e32 v24, v24
	v_exp_f32_e32 v25, v25
	v_exp_f32_e32 v26, v26
	v_exp_f32_e32 v27, v27
	v_cvt_pk_f16_f32 v46, v20, v21
	v_cvt_pk_f16_f32 v47, v22, v23
	v_cvt_pk_f16_f32 v78, v24, v25
	v_cvt_pk_f16_f32 v79, v26, v27
	v_add_u32_e32 v6, 0x8000, v6
	global_load_dwordx4 v[240:243], v6, s[12:13] offset:0 nt
	global_load_dwordx4 v[244:247], v6, s[12:13] offset:1024 nt
	global_load_dwordx4 v[248:251], v6, s[12:13] offset:2048 nt
	global_load_dwordx4 v[252:255], v6, s[12:13] offset:3072 nt
	v_add_f32_e32 v16, 0x42800000, v12
	v_add_f32_e32 v17, 0x42820000, v12
	v_add_f32_e32 v18, 0x42840000, v12
	v_add_f32_e32 v19, 0x42860000, v12
	v_mul_f32_e32 v16, v16, v16
	v_mul_f32_e32 v17, v17, v17
	v_mul_f32_e32 v18, v18, v18
	v_mul_f32_e32 v19, v19, v19
	v_mul_f32_e32 v20, v8, v16
	v_mul_f32_e32 v24, v9, v16
	v_mul_f32_e32 v21, v8, v17
	v_mul_f32_e32 v25, v9, v17
	v_mul_f32_e32 v22, v8, v18
	v_mul_f32_e32 v26, v9, v18
	v_mul_f32_e32 v23, v8, v19
	v_mul_f32_e32 v27, v9, v19
	v_exp_f32_e32 v20, v20
	v_exp_f32_e32 v21, v21
	v_exp_f32_e32 v22, v22
	v_exp_f32_e32 v23, v23
	v_exp_f32_e32 v24, v24
	v_exp_f32_e32 v25, v25
	v_exp_f32_e32 v26, v26
	v_exp_f32_e32 v27, v27
	v_cvt_pk_f16_f32 v48, v20, v21
	v_cvt_pk_f16_f32 v49, v22, v23
	v_cvt_pk_f16_f32 v80, v24, v25
	v_cvt_pk_f16_f32 v81, v26, v27
	v_add_f32_e32 v16, 0x42880000, v12
	v_add_f32_e32 v17, 0x428a0000, v12
	v_add_f32_e32 v18, 0x428c0000, v12
	v_add_f32_e32 v19, 0x428e0000, v12
	v_mul_f32_e32 v16, v16, v16
	v_mul_f32_e32 v17, v17, v17
	v_mul_f32_e32 v18, v18, v18
	v_mul_f32_e32 v19, v19, v19
	v_mul_f32_e32 v20, v8, v16
	v_mul_f32_e32 v24, v9, v16
	v_mul_f32_e32 v21, v8, v17
	v_mul_f32_e32 v25, v9, v17
	v_mul_f32_e32 v22, v8, v18
	v_mul_f32_e32 v26, v9, v18
	v_mul_f32_e32 v23, v8, v19
	v_mul_f32_e32 v27, v9, v19
	v_exp_f32_e32 v20, v20
	v_exp_f32_e32 v21, v21
	v_exp_f32_e32 v22, v22
	v_exp_f32_e32 v23, v23
	v_exp_f32_e32 v24, v24
	v_exp_f32_e32 v25, v25
	v_exp_f32_e32 v26, v26
	v_exp_f32_e32 v27, v27
	v_cvt_pk_f16_f32 v50, v20, v21
	v_cvt_pk_f16_f32 v51, v22, v23
	v_cvt_pk_f16_f32 v82, v24, v25
	v_cvt_pk_f16_f32 v83, v26, v27
	v_add_f32_e32 v16, 0x42a00000, v12
	v_add_f32_e32 v17, 0x42a20000, v12
	v_add_f32_e32 v18, 0x42a40000, v12
	v_add_f32_e32 v19, 0x42a60000, v12
	v_mul_f32_e32 v16, v16, v16
	v_mul_f32_e32 v17, v17, v17
	v_mul_f32_e32 v18, v18, v18
	v_mul_f32_e32 v19, v19, v19
	v_mul_f32_e32 v20, v8, v16
	v_mul_f32_e32 v24, v9, v16
	v_mul_f32_e32 v21, v8, v17
	v_mul_f32_e32 v25, v9, v17
	v_mul_f32_e32 v22, v8, v18
	v_mul_f32_e32 v26, v9, v18
	v_mul_f32_e32 v23, v8, v19
	v_mul_f32_e32 v27, v9, v19
	v_exp_f32_e32 v20, v20
	v_exp_f32_e32 v21, v21
	v_exp_f32_e32 v22, v22
	v_exp_f32_e32 v23, v23
	v_exp_f32_e32 v24, v24
	v_exp_f32_e32 v25, v25
	v_exp_f32_e32 v26, v26
	v_exp_f32_e32 v27, v27
	v_cvt_pk_f16_f32 v52, v20, v21
	v_cvt_pk_f16_f32 v53, v22, v23
	v_cvt_pk_f16_f32 v84, v24, v25
	v_cvt_pk_f16_f32 v85, v26, v27
	v_add_f32_e32 v16, 0x42a80000, v12
	v_add_f32_e32 v17, 0x42aa0000, v12
	v_add_f32_e32 v18, 0x42ac0000, v12
	v_add_f32_e32 v19, 0x42ae0000, v12
	v_mul_f32_e32 v16, v16, v16
	v_mul_f32_e32 v17, v17, v17
	v_mul_f32_e32 v18, v18, v18
	v_mul_f32_e32 v19, v19, v19
	v_mul_f32_e32 v20, v8, v16
	v_mul_f32_e32 v24, v9, v16
	v_mul_f32_e32 v21, v8, v17
	v_mul_f32_e32 v25, v9, v17
	v_mul_f32_e32 v22, v8, v18
	v_mul_f32_e32 v26, v9, v18
	v_mul_f32_e32 v23, v8, v19
	v_mul_f32_e32 v27, v9, v19
	v_exp_f32_e32 v20, v20
	v_exp_f32_e32 v21, v21
	v_exp_f32_e32 v22, v22
	v_exp_f32_e32 v23, v23
	v_exp_f32_e32 v24, v24
	v_exp_f32_e32 v25, v25
	v_exp_f32_e32 v26, v26
	v_exp_f32_e32 v27, v27
	v_cvt_pk_f16_f32 v54, v20, v21
	v_cvt_pk_f16_f32 v55, v22, v23
	v_cvt_pk_f16_f32 v86, v24, v25
	v_cvt_pk_f16_f32 v87, v26, v27
	v_add_f32_e32 v16, 0x42c00000, v12
	v_add_f32_e32 v17, 0x42c20000, v12
	v_add_f32_e32 v18, 0x42c40000, v12
	v_add_f32_e32 v19, 0x42c60000, v12
	v_mul_f32_e32 v16, v16, v16
	v_mul_f32_e32 v17, v17, v17
	v_mul_f32_e32 v18, v18, v18
	v_mul_f32_e32 v19, v19, v19
	v_mul_f32_e32 v20, v8, v16
	v_mul_f32_e32 v24, v9, v16
	v_mul_f32_e32 v21, v8, v17
	v_mul_f32_e32 v25, v9, v17
	v_mul_f32_e32 v22, v8, v18
	v_mul_f32_e32 v26, v9, v18
	v_mul_f32_e32 v23, v8, v19
	v_mul_f32_e32 v27, v9, v19
	v_exp_f32_e32 v20, v20
	v_exp_f32_e32 v21, v21
	v_exp_f32_e32 v22, v22
	v_exp_f32_e32 v23, v23
	v_exp_f32_e32 v24, v24
	v_exp_f32_e32 v25, v25
	v_exp_f32_e32 v26, v26
	v_exp_f32_e32 v27, v27
	v_cvt_pk_f16_f32 v56, v20, v21
	v_cvt_pk_f16_f32 v57, v22, v23
	v_cvt_pk_f16_f32 v88, v24, v25
	v_cvt_pk_f16_f32 v89, v26, v27
	v_add_f32_e32 v16, 0x42c80000, v12
	v_add_f32_e32 v17, 0x42ca0000, v12
	v_add_f32_e32 v18, 0x42cc0000, v12
	v_add_f32_e32 v19, 0x42ce0000, v12
	v_mul_f32_e32 v16, v16, v16
	v_mul_f32_e32 v17, v17, v17
	v_mul_f32_e32 v18, v18, v18
	v_mul_f32_e32 v19, v19, v19
	v_mul_f32_e32 v20, v8, v16
	v_mul_f32_e32 v24, v9, v16
	v_mul_f32_e32 v21, v8, v17
	v_mul_f32_e32 v25, v9, v17
	v_mul_f32_e32 v22, v8, v18
	v_mul_f32_e32 v26, v9, v18
	v_mul_f32_e32 v23, v8, v19
	v_mul_f32_e32 v27, v9, v19
	v_exp_f32_e32 v20, v20
	v_exp_f32_e32 v21, v21
	v_exp_f32_e32 v22, v22
	v_exp_f32_e32 v23, v23
	v_exp_f32_e32 v24, v24
	v_exp_f32_e32 v25, v25
	v_exp_f32_e32 v26, v26
	v_exp_f32_e32 v27, v27
	v_cvt_pk_f16_f32 v58, v20, v21
	v_cvt_pk_f16_f32 v59, v22, v23
	v_cvt_pk_f16_f32 v90, v24, v25
	v_cvt_pk_f16_f32 v91, v26, v27
	v_add_f32_e32 v16, 0x42e00000, v12
	v_add_f32_e32 v17, 0x42e20000, v12
	v_add_f32_e32 v18, 0x42e40000, v12
	v_add_f32_e32 v19, 0x42e60000, v12
	v_mul_f32_e32 v16, v16, v16
	v_mul_f32_e32 v17, v17, v17
	v_mul_f32_e32 v18, v18, v18
	v_mul_f32_e32 v19, v19, v19
	v_mul_f32_e32 v20, v8, v16
	v_mul_f32_e32 v24, v9, v16
	v_mul_f32_e32 v21, v8, v17
	v_mul_f32_e32 v25, v9, v17
	v_mul_f32_e32 v22, v8, v18
	v_mul_f32_e32 v26, v9, v18
	v_mul_f32_e32 v23, v8, v19
	v_mul_f32_e32 v27, v9, v19
	v_exp_f32_e32 v20, v20
	v_exp_f32_e32 v21, v21
	v_exp_f32_e32 v22, v22
	v_exp_f32_e32 v23, v23
	v_exp_f32_e32 v24, v24
	v_exp_f32_e32 v25, v25
	v_exp_f32_e32 v26, v26
	v_exp_f32_e32 v27, v27
	v_cvt_pk_f16_f32 v60, v20, v21
	v_cvt_pk_f16_f32 v61, v22, v23
	v_cvt_pk_f16_f32 v92, v24, v25
	v_cvt_pk_f16_f32 v93, v26, v27
	v_add_f32_e32 v16, 0x42e80000, v12
	v_add_f32_e32 v17, 0x42ea0000, v12
	v_add_f32_e32 v18, 0x42ec0000, v12
	v_add_f32_e32 v19, 0x42ee0000, v12
	v_mul_f32_e32 v16, v16, v16
	v_mul_f32_e32 v17, v17, v17
	v_mul_f32_e32 v18, v18, v18
	v_mul_f32_e32 v19, v19, v19
	v_mul_f32_e32 v20, v8, v16
	v_mul_f32_e32 v24, v9, v16
	v_mul_f32_e32 v21, v8, v17
	v_mul_f32_e32 v25, v9, v17
	v_mul_f32_e32 v22, v8, v18
	v_mul_f32_e32 v26, v9, v18
	v_mul_f32_e32 v23, v8, v19
	v_mul_f32_e32 v27, v9, v19
	v_exp_f32_e32 v20, v20
	v_exp_f32_e32 v21, v21
	v_exp_f32_e32 v22, v22
	v_exp_f32_e32 v23, v23
	v_exp_f32_e32 v24, v24
	v_exp_f32_e32 v25, v25
	v_exp_f32_e32 v26, v26
	v_exp_f32_e32 v27, v27
	v_cvt_pk_f16_f32 v62, v20, v21
	v_cvt_pk_f16_f32 v63, v22, v23
	v_cvt_pk_f16_f32 v94, v24, v25
	v_cvt_pk_f16_f32 v95, v26, v27
	v_mul_f32_e32 v16, v13, v13
	v_add_f32_e32 v17, 0x3f800000, v13
	v_add_f32_e32 v18, 0x40000000, v13
	v_add_f32_e32 v19, 0x40400000, v13
	v_mul_f32_e32 v17, v17, v17
	v_mul_f32_e32 v18, v18, v18
	v_mul_f32_e32 v19, v19, v19
	v_mul_f32_e32 v20, v8, v16
	v_mul_f32_e32 v24, v9, v16
	v_mul_f32_e32 v21, v8, v17
	v_mul_f32_e32 v25, v9, v17
	v_mul_f32_e32 v22, v8, v18
	v_mul_f32_e32 v26, v9, v18
	v_mul_f32_e32 v23, v8, v19
	v_mul_f32_e32 v27, v9, v19
	v_exp_f32_e32 v20, v20
	v_exp_f32_e32 v21, v21
	v_exp_f32_e32 v22, v22
	v_exp_f32_e32 v23, v23
	v_exp_f32_e32 v24, v24
	v_exp_f32_e32 v25, v25
	v_exp_f32_e32 v26, v26
	v_exp_f32_e32 v27, v27
	v_mul_f32_e32 v96, v10, v20
	v_mul_f32_e32 v97, v10, v21
	v_mul_f32_e32 v98, v10, v22
	v_mul_f32_e32 v99, v10, v23
	v_mul_f32_e32 v112, v11, v24
	v_mul_f32_e32 v113, v11, v25
	v_mul_f32_e32 v114, v11, v26
	v_mul_f32_e32 v115, v11, v27
	v_add_f32_e32 v16, 0x41000000, v13
	v_add_f32_e32 v17, 0x41100000, v13
	v_add_f32_e32 v18, 0x41200000, v13
	v_add_f32_e32 v19, 0x41300000, v13
	v_mul_f32_e32 v16, v16, v16
	v_mul_f32_e32 v17, v17, v17
	v_mul_f32_e32 v18, v18, v18
	v_mul_f32_e32 v19, v19, v19
	v_mul_f32_e32 v20, v8, v16
	v_mul_f32_e32 v24, v9, v16
	v_mul_f32_e32 v21, v8, v17
	v_mul_f32_e32 v25, v9, v17
	v_mul_f32_e32 v22, v8, v18
	v_mul_f32_e32 v26, v9, v18
	v_mul_f32_e32 v23, v8, v19
	v_mul_f32_e32 v27, v9, v19
	v_exp_f32_e32 v20, v20
	v_exp_f32_e32 v21, v21
	v_exp_f32_e32 v22, v22
	v_exp_f32_e32 v23, v23
	v_exp_f32_e32 v24, v24
	v_exp_f32_e32 v25, v25
	v_exp_f32_e32 v26, v26
	v_exp_f32_e32 v27, v27
	v_mul_f32_e32 v100, v10, v20
	v_mul_f32_e32 v101, v10, v21
	v_mul_f32_e32 v102, v10, v22
	v_mul_f32_e32 v103, v10, v23
	v_mul_f32_e32 v116, v11, v24
	v_mul_f32_e32 v117, v11, v25
	v_mul_f32_e32 v118, v11, v26
	v_mul_f32_e32 v119, v11, v27
	v_add_f32_e32 v16, 0x41800000, v13
	v_add_f32_e32 v17, 0x41880000, v13
	v_add_f32_e32 v18, 0x41900000, v13
	v_add_f32_e32 v19, 0x41980000, v13
	v_mul_f32_e32 v16, v16, v16
	v_mul_f32_e32 v17, v17, v17
	v_mul_f32_e32 v18, v18, v18
	v_mul_f32_e32 v19, v19, v19
	v_mul_f32_e32 v20, v8, v16
	v_mul_f32_e32 v24, v9, v16
	v_mul_f32_e32 v21, v8, v17
	v_mul_f32_e32 v25, v9, v17
	v_mul_f32_e32 v22, v8, v18
	v_mul_f32_e32 v26, v9, v18
	v_mul_f32_e32 v23, v8, v19
	v_mul_f32_e32 v27, v9, v19
	v_exp_f32_e32 v20, v20
	v_exp_f32_e32 v21, v21
	v_exp_f32_e32 v22, v22
	v_exp_f32_e32 v23, v23
	v_exp_f32_e32 v24, v24
	v_exp_f32_e32 v25, v25
	v_exp_f32_e32 v26, v26
	v_exp_f32_e32 v27, v27
	v_mul_f32_e32 v104, v10, v20
	v_mul_f32_e32 v105, v10, v21
	v_mul_f32_e32 v106, v10, v22
	v_mul_f32_e32 v107, v10, v23
	v_mul_f32_e32 v120, v11, v24
	v_mul_f32_e32 v121, v11, v25
	v_mul_f32_e32 v122, v11, v26
	v_mul_f32_e32 v123, v11, v27
	v_add_f32_e32 v16, 0x41c00000, v13
	v_add_f32_e32 v17, 0x41c80000, v13
	v_add_f32_e32 v18, 0x41d00000, v13
	v_add_f32_e32 v19, 0x41d80000, v13
	v_mul_f32_e32 v16, v16, v16
	v_mul_f32_e32 v17, v17, v17
	v_mul_f32_e32 v18, v18, v18
	v_mul_f32_e32 v19, v19, v19
	v_mul_f32_e32 v20, v8, v16
	v_mul_f32_e32 v24, v9, v16
	v_mul_f32_e32 v21, v8, v17
	v_mul_f32_e32 v25, v9, v17
	v_mul_f32_e32 v22, v8, v18
	v_mul_f32_e32 v26, v9, v18
	v_mul_f32_e32 v23, v8, v19
	v_mul_f32_e32 v27, v9, v19
	v_exp_f32_e32 v20, v20
	v_exp_f32_e32 v21, v21
	v_exp_f32_e32 v22, v22
	v_exp_f32_e32 v23, v23
	v_exp_f32_e32 v24, v24
	v_exp_f32_e32 v25, v25
	v_exp_f32_e32 v26, v26
	v_exp_f32_e32 v27, v27
	v_mul_f32_e32 v108, v10, v20
	v_mul_f32_e32 v109, v10, v21
	v_mul_f32_e32 v110, v10, v22
	v_mul_f32_e32 v111, v10, v23
	v_mul_f32_e32 v124, v11, v24
	v_mul_f32_e32 v125, v11, v25
	v_mul_f32_e32 v126, v11, v26
	v_mul_f32_e32 v127, v11, v27
